# P5 m3 unit: q tile staged once into LDS (row pad placed over the grid-barrier words); the stage-2 loop reads its q fragments from LDS instead of 4 scattered global loads per trip
# speedup vs baseline: 1.0177x; 1.0000x over previous
.LBB0_759:
	s_ashr_i32 s54, s52, 8
	s_ashr_i32 s55, s54, 31
	s_lshl_b32 s53, s52, 7
	s_ashr_i32 vcc_lo, s52, 6
	s_lshl_b64 s[58:59], s[54:55], 13
	s_and_b32 s96, s53, 0x1f80
	s_and_b32 s49, vcc_lo, 3
	s_or_b32 s54, s58, s96
	s_mov_b32 s55, s59
	s_lshl_b32 s56, s49, 8
	s_mov_b32 s57, s97
	v_lshl_add_u64 v[0:1], s[54:55], 0, v[92:93]
	v_lshl_add_u64 v[4:5], v[90:91], 0, s[56:57]
	v_lshlrev_b64 v[0:1], 10, v[0:1]
	v_lshl_add_u64 v[0:1], v[4:5], 0, v[0:1]
	global_load_dwordx4 v[52:55], v[0:1], off
	s_mov_b32 s74, 0xff000000
	s_mov_b32 s75, -1
	v_lshl_add_u64 v[72:73], v[0:1], 0, s[74:75]
	global_load_dwordx4 v[56:59], v[72:73], off
	s_lshl_b32 s53, s49, 9
	s_add_u32 s60, s88, s53
	s_addc_u32 s61, s89, 0
	v_mov_b32_e32 v137, v85
	s_ashr_i32 s53, s52, 31
	v_lshl_add_u64 v[0:1], s[54:55], 0, v[94:95]
	v_lshlrev_b64 v[0:1], 10, v[0:1]
	v_lshl_add_u64 v[0:1], v[4:5], 0, v[0:1]
	global_load_dwordx4 v[8:11], v[0:1], off
	v_lshl_add_u64 v[72:73], v[0:1], 0, s[74:75]
	global_load_dwordx4 v[60:63], v[72:73], off
	v_lshl_add_u64 v[0:1], s[54:55], 0, v[96:97]
	v_lshlrev_b64 v[0:1], 10, v[0:1]
	v_lshl_add_u64 v[0:1], v[4:5], 0, v[0:1]
	global_load_dwordx4 v[12:15], v[0:1], off
	v_lshl_add_u64 v[72:73], v[0:1], 0, s[74:75]
	global_load_dwordx4 v[64:67], v[72:73], off
	v_lshl_add_u64 v[0:1], s[54:55], 0, v[98:99]
	v_lshlrev_b64 v[0:1], 10, v[0:1]
	v_lshl_add_u64 v[0:1], v[4:5], 0, v[0:1]
	global_load_dwordx4 v[16:19], v[0:1], off
	v_lshl_add_u64 v[72:73], v[0:1], 0, s[74:75]
	global_load_dwordx4 v[68:71], v[72:73], off
	v_lshl_add_u64 v[0:1], s[60:61], 0, v[136:137]
	s_mov_b64 s[60:61], 0x1200
	v_lshl_add_u64 v[4:5], v[0:1], 0, s[60:61]
	v_lshl_add_u64 v[0:1], s[54:55], 0, v[100:101]
	v_mad_u64_u32 v[2:3], s[60:61], v0, s65, v[4:5]
	v_mad_i32_i24 v3, v1, s65, v3
	global_load_dwordx4 v[20:23], v[2:3], off
	v_lshl_add_u64 v[0:1], s[54:55], 0, v[102:103]
	v_mad_u64_u32 v[2:3], s[60:61], v0, s65, v[4:5]
	v_mad_i32_i24 v3, v1, s65, v3
	global_load_dwordx4 v[24:27], v[2:3], off
	v_lshl_add_u64 v[0:1], s[54:55], 0, v[104:105]
	v_mad_u64_u32 v[2:3], s[60:61], v0, s65, v[4:5]
	v_mad_i32_i24 v3, v1, s65, v3
	global_load_dwordx4 v[28:31], v[2:3], off
	v_lshl_add_u64 v[0:1], s[54:55], 0, v[106:107]
	v_mad_u64_u32 v[2:3], s[60:61], v0, s65, v[4:5]
	v_mad_i32_i24 v3, v1, s65, v3
	global_load_dwordx4 v[32:35], v[2:3], off
	v_lshl_add_u64 v[0:1], s[54:55], 0, v[108:109]
	v_mad_u64_u32 v[2:3], s[60:61], v0, s65, v[4:5]
	v_mad_i32_i24 v3, v1, s65, v3
	global_load_dwordx4 v[36:39], v[2:3], off
	v_lshl_add_u64 v[0:1], s[54:55], 0, v[110:111]
	v_mad_u64_u32 v[2:3], s[60:61], v0, s65, v[4:5]
	v_mad_i32_i24 v3, v1, s65, v3
	global_load_dwordx4 v[40:43], v[2:3], off
	v_lshl_add_u64 v[0:1], s[54:55], 0, v[112:113]
	v_mad_u64_u32 v[2:3], s[60:61], v0, s65, v[4:5]
	v_mad_i32_i24 v3, v1, s65, v3
	global_load_dwordx4 v[44:47], v[2:3], off
	v_lshl_add_u64 v[0:1], s[54:55], 0, v[114:115]
	v_mad_u64_u32 v[2:3], s[60:61], v0, s65, v[4:5]
	v_mad_i32_i24 v3, v1, s65, v3
	global_load_dwordx4 v[48:51], v[2:3], off
	s_lshl_b64 s[60:61], s[52:53], 2
	s_add_u32 s60, s33, s60
	s_addc_u32 s61, s62, s61
	s_waitcnt vmcnt(15)
	ds_write_b128 v182, v[52:55]
	s_waitcnt vmcnt(13)
	ds_write_b128 v183, v[8:11]
	s_waitcnt vmcnt(11)
	ds_write_b128 v184, v[12:15]
	s_waitcnt vmcnt(9)
	ds_write_b128 v185, v[16:19]
	s_waitcnt vmcnt(7)
	ds_write_b128 v186, v[20:23] offset:34816
	s_waitcnt vmcnt(6)
	ds_write_b128 v187, v[24:27] offset:34816
	s_waitcnt vmcnt(5)
	ds_write_b128 v188, v[28:31] offset:34816
	s_waitcnt vmcnt(4)
	ds_write_b128 v189, v[32:35] offset:34816
	s_waitcnt vmcnt(3)
	ds_write_b128 v190, v[36:39] offset:34816
	s_waitcnt vmcnt(2)
	ds_write_b128 v191, v[40:43] offset:34816
	s_waitcnt vmcnt(1)
	ds_write_b128 v192, v[44:47] offset:34816
	s_waitcnt vmcnt(0)
	ds_write_b128 v193, v[48:51] offset:34816
	v_add_u32_e32 v74, 0x1b810, v182
	ds_write_b128 v74, v[56:59]
	v_add_u32_e32 v74, 0x1b810, v183
	ds_write_b128 v74, v[60:63]
	v_add_u32_e32 v74, 0x1b810, v184
	ds_write_b128 v74, v[64:67]
	v_add_u32_e32 v74, 0x1b810, v185
	ds_write_b128 v74, v[68:71]
	global_load_dword v0, v85, s[60:61]
	v_mov_b32_e32 v2, 0xff800000
	v_mov_b32_e32 v1, v85
	s_and_saveexec_b64 s[60:61], s[16:17]
	s_cbranch_execz .LBB0_761
	s_ashr_i32 vcc_hi, vcc_lo, 31
	s_lshl_b64 s[74:75], vcc, 13
	s_or_b64 s[74:75], s[74:75], s[96:97]
	v_lshl_add_u64 v[2:3], s[74:75], 0, v[88:89]
	v_lshlrev_b64 v[2:3], 2, v[2:3]
	v_lshl_add_u64 v[4:5], s[44:45], 0, v[2:3]
	v_lshl_add_u64 v[2:3], s[46:47], 0, v[2:3]
	s_lshl_b64 s[74:75], s[52:53], 9
	global_load_dword v1, v[4:5], off
	s_nop 0
	global_load_dword v2, v[2:3], off
	v_lshl_add_u64 v[4:5], v[128:129], 0, s[74:75]
	global_load_dword v3, v[4:5], off
	s_waitcnt vmcnt(1)
	v_sub_f32_e32 v2, v2, v1
	s_waitcnt vmcnt(0)
	ds_write_b32 v168, v3

.LBB0_786:
	s_or_b64 exec, exec, s[60:61]
	s_waitcnt lgkmcnt(0)
	v_and_b32_sdwa v1, v33, v198 dst_sel:DWORD dst_unused:UNUSED_PAD src0_sel:WORD_1 src1_sel:DWORD
	v_add3_u32 v2, v33, v1, s71
	v_and_b32_sdwa v1, v34, v198 dst_sel:DWORD dst_unused:UNUSED_PAD src0_sel:WORD_1 src1_sel:DWORD
	v_and_b32_sdwa v3, v35, v198 dst_sel:DWORD dst_unused:UNUSED_PAD src0_sel:WORD_1 src1_sel:DWORD
	v_and_b32_sdwa v0, v32, v198 dst_sel:DWORD dst_unused:UNUSED_PAD src0_sel:WORD_1 src1_sel:DWORD
	v_add3_u32 v1, v34, v1, s71
	v_add3_u32 v3, v35, v3, s71
	v_mov_b32_e32 v147, s55
	v_or_b32_e32 v146, s54, v86
	v_add3_u32 v0, v32, v0, s71
	v_and_b32_e32 v1, 0xffff0000, v1
	v_and_b32_e32 v3, 0xffff0000, v3
	v_lshlrev_b64 v[32:33], 10, v[146:147]
	v_or_b32_sdwa v1, v1, v0 dst_sel:DWORD dst_unused:UNUSED_PAD src0_sel:DWORD src1_sel:WORD_1
	v_or_b32_sdwa v0, v3, v2 dst_sel:DWORD dst_unused:UNUSED_PAD src0_sel:DWORD src1_sel:WORD_1
	s_lshl_b64 s[60:61], s[52:53], 16
	v_lshl_add_u64 v[32:33], s[0:1], 0, v[32:33]
	s_barrier
	ds_write2_b64 v164, v[0:1], v[22:23] offset1:4
	ds_write2_b64 v164, v[20:21], v[26:27] offset0:8 offset1:12
	ds_write2_b64 v164, v[24:25], v[30:31] offset0:16 offset1:20
	ds_write2_b64 v164, v[28:29], v[16:17] offset0:24 offset1:28
	v_lshl_add_u64 v[16:17], v[120:121], 0, s[60:61]
	v_lshl_add_u64 v[32:33], v[32:33], 0, s[96:97]
	v_mov_b32_e32 v141, v85
	v_lshl_add_u64 v[12:13], v[16:17], 0, v[122:123]
	v_lshl_add_u64 v[28:29], v[16:17], 0, v[124:125]
	v_lshl_add_u64 v[32:33], v[32:33], 0, v[140:141]
	s_waitcnt lgkmcnt(0)
	s_barrier
	global_load_dwordx4 v[0:3], v[12:13], off
	global_load_dwordx4 v[4:7], v[12:13], off offset:64
	global_load_dwordx4 v[8:11], v[12:13], off offset:128
	s_nop 0
	global_load_dwordx4 v[12:15], v[12:13], off offset:192
	s_nop 0
	global_load_dwordx4 v[16:19], v[28:29], off
	global_load_dwordx4 v[20:23], v[28:29], off offset:64
	global_load_dwordx4 v[24:27], v[28:29], off offset:128
	s_nop 0
	global_load_dwordx4 v[28:31], v[28:29], off offset:192
	s_nop 0
	v_mbcnt_lo_u32_b32 v242, -1, 0
	v_mbcnt_hi_u32_b32 v242, -1, v242
	v_and_b32_e32 v243, 15, v242
	v_lshrrev_b32_e32 v242, 4, v242
	v_lshlrev_b32_e32 v242, 4, v242
	v_mul_u32_u24_e32 v243, 0x110, v243
	v_add_u32_e32 v242, v242, v243
	v_add_u32_e32 v242, 0x1b810, v242
	ds_read_b128 v[68:71], v242
	ds_read_b128 v[60:63], v242 offset:64
	ds_read_b128 v[72:75], v242 offset:128
	ds_read_b128 v[76:79], v242 offset:192
	ds_read_b64_tr_b16 v[34:35], v165 offset:36992
	ds_read_b64_tr_b16 v[32:33], v165 offset:34816
	ds_read_b64_tr_b16 v[38:39], v165 offset:37024
	ds_read_b64_tr_b16 v[36:37], v165 offset:34848
	ds_read_b64_tr_b16 v[40:41], v166 offset:34816
	ds_read_b64_tr_b16 v[42:43], v166 offset:36992
	ds_read_b64_tr_b16 v[44:45], v166 offset:52224
	ds_read_b64_tr_b16 v[46:47], v166 offset:54400
	ds_read_b64_tr_b16 v[48:49], v165 offset:52224
	ds_read_b64_tr_b16 v[50:51], v165 offset:54400
	ds_read_b64_tr_b16 v[54:55], v165 offset:54432
	ds_read_b64_tr_b16 v[52:53], v165 offset:52256
	ds_read_b64_tr_b16 v[56:57], v167 offset:34816
	ds_read_b64_tr_b16 v[58:59], v167 offset:36992
	ds_read_b64_tr_b16 v[64:65], v167 offset:52224
	ds_read_b64_tr_b16 v[66:67], v167 offset:54400
	s_and_b32 s53, s63, 0x1f80
	s_add_u32 s58, s53, s58
	s_addc_u32 s59, 0, s59
	v_lshl_add_u64 v[80:81], s[58:59], 0, v[86:87]
	s_lshl_b32 s53, s52, 3
	v_lshlrev_b64 v[144:145], 11, v[80:81]
	s_and_b32 s53, s53, 0x600
	v_or_b32_e32 v144, s53, v144
	s_mov_b32 s49, 16
	v_lshl_add_u64 v[148:149], v[126:127], 0, s[96:97]
	v_lshl_add_u64 v[150:151], v[132:133], 0, v[144:145]
	s_mov_b64 s[58:59], 0
	v_mov_b32_e32 v84, v180
	v_mov_b32_e32 v137, v179
	v_mov_b32_e32 v139, v178
	v_mbcnt_lo_u32_b32 v240, -1, 0
	v_mbcnt_hi_u32_b32 v240, -1, v240
	v_lshlrev_b32_e32 v240, 3, v240
	v_readlane_b32 s32, v252, 1
	s_lshl_b32 s32, s32, 13
	v_add_u32_e32 v240, s32, v240
	v_add_u32_e32 v240, 0x8800, v240
	s_waitcnt lgkmcnt(0)
	s_barrier
	s_branch .LBB0_788

.LBB0_788:
	v_add_u32_e32 v141, 0, v84
	ds_read_b128 v[200:203], v141
	ds_read_b128 v[204:207], v141 offset:64
	s_waitcnt vmcnt(0)
	v_mov_b64_e32 v[210:211], v[70:71]
	v_mov_b64_e32 v[208:209], v[68:69]
	s_waitcnt vmcnt(2)
	v_mov_b64_e32 v[218:219], v[62:63]
	s_waitcnt lgkmcnt(1)
	v_mfma_f32_16x16x32_bf16 v[80:83], v[32:35], v[200:203], 0
	s_waitcnt vmcnt(1)
	v_mov_b64_e32 v[214:215], v[74:75]
	v_mov_b64_e32 v[216:217], v[60:61]
	s_cmp_lg_u32 s58, 0x38000
	v_mfma_f32_16x16x32_bf16 v[68:71], v[0:3], v[208:211], 0
	ds_read_b128 v[220:223], v141 offset:128
	ds_read_b128 v[224:227], v141 offset:192
	v_mov_b64_e32 v[212:213], v[72:73]
	s_waitcnt lgkmcnt(2)
	v_mfma_f32_16x16x32_bf16 v[60:63], v[48:51], v[204:207], v[80:83]
	s_cselect_b32 s96, s49, 0x70
	s_mul_i32 s32, s96, 0x110
	v_add_u32_e32 v243, s32, v242
	v_add_u32_e32 v141, 0, v137
	v_add_u32_e32 v143, 0x19c00, v141
	v_mfma_f32_16x16x32_bf16 v[72:75], v[4:7], v[216:219], v[68:71]
	v_add_u32_e32 v141, 0x19e00, v141
	s_nop 1
	v_lshl_add_u64 v[68:69], v[146:147], 0, s[96:97]
	v_lshlrev_b64 v[68:69], 10, v[68:69]
	v_lshl_add_u64 v[80:81], v[148:149], 0, v[68:69]
	s_waitcnt lgkmcnt(1)
	v_mfma_f32_16x16x32_bf16 v[228:231], v[40:43], v[220:223], v[60:63]
	ds_read_b128 v[68:71], v243
	s_nop 1
	ds_read_b128 v[60:63], v243 offset:64
	v_mfma_f32_16x16x32_bf16 v[232:235], v[8:11], v[212:215], v[72:75]
	s_nop 2
	ds_read_b128 v[72:75], v243 offset:128
	s_nop 0
	ds_read_b128 v[80:83], v243 offset:192
	ds_read_b32 v236, v143
	ds_read_b32 v238, v141
	v_mfma_f32_16x16x32_bf16 v[200:203], v[36:39], v[200:203], 0
	v_mfma_f32_16x16x32_bf16 v[208:211], v[16:19], v[208:211], 0
	v_mfma_f32_16x16x32_bf16 v[200:203], v[52:55], v[204:207], v[200:203]
	v_mfma_f32_16x16x32_bf16 v[204:207], v[20:23], v[216:219], v[208:211]
	s_waitcnt lgkmcnt(6)
	v_mfma_f32_16x16x32_bf16 v[228:231], v[44:47], v[224:227], v[228:231]
	s_waitcnt vmcnt(4)
	v_mfma_f32_16x16x32_bf16 v[232:235], v[12:15], v[76:79], v[232:235]
	v_mfma_f32_16x16x32_bf16 v[200:203], v[56:59], v[220:223], v[200:203]
	v_mfma_f32_16x16x32_bf16 v[204:207], v[24:27], v[212:215], v[204:207]
	s_waitcnt lgkmcnt(1)
	s_nop 4
	v_pk_fma_f32 v[230:231], v[236:237], v[234:235], v[230:231] op_sel_hi:[0,1,1]
	v_pk_fma_f32 v[228:229], v[236:237], v[232:233], v[228:229] op_sel_hi:[0,1,1]
	s_waitcnt lgkmcnt(0)
	v_pk_mul_f32 v[230:231], v[238:239], v[230:231] op_sel_hi:[0,1]
	v_mfma_f32_16x16x32_bf16 v[200:203], v[64:67], v[224:227], v[200:203]
	v_mul_f32_e64 v228, v238, v228
	v_mul_f32_e64 v229, v238, v229
	v_mul_f32_e32 v141, v229, v229
	v_mul_f32_e32 v143, v231, v231
	v_mfma_f32_16x16x32_bf16 v[76:79], v[28:31], v[76:79], v[204:207]
	v_fmac_f32_e32 v141, v228, v228
	v_fmac_f32_e32 v143, v230, v230
	v_and_b32_sdwa v208, v231, v198 dst_sel:DWORD dst_unused:UNUSED_PAD src0_sel:WORD_1 src1_sel:DWORD
	v_and_b32_sdwa v209, v229, v198 dst_sel:DWORD dst_unused:UNUSED_PAD src0_sel:WORD_1 src1_sel:DWORD
	v_add_f32_e32 v141, v141, v143
	v_and_b32_sdwa v143, v230, v198 dst_sel:DWORD dst_unused:UNUSED_PAD src0_sel:WORD_1 src1_sel:DWORD
	v_and_b32_sdwa v199, v228, v198 dst_sel:DWORD dst_unused:UNUSED_PAD src0_sel:WORD_1 src1_sel:DWORD
	v_add3_u32 v208, v231, v208, s71
	v_add3_u32 v209, v229, v209, s71
	v_pk_fma_f32 v[78:79], v[236:237], v[78:79], v[202:203] op_sel_hi:[0,1,1]
	v_pk_fma_f32 v[76:77], v[236:237], v[76:77], v[200:201] op_sel_hi:[0,1,1]
	v_add3_u32 v199, v228, v199, s71
	v_add3_u32 v143, v230, v143, s71
	v_and_b32_e32 v208, 0xffff0000, v208
	v_and_b32_e32 v210, 0xffff0000, v209
	v_pk_mul_f32 v[78:79], v[238:239], v[78:79] op_sel_hi:[0,1]
	v_pk_mul_f32 v[76:77], v[238:239], v[76:77] op_sel_hi:[0,1]
	v_or_b32_sdwa v209, v208, v143 dst_sel:DWORD dst_unused:UNUSED_PAD src0_sel:DWORD src1_sel:WORD_1
	v_or_b32_sdwa v208, v210, v199 dst_sel:DWORD dst_unused:UNUSED_PAD src0_sel:DWORD src1_sel:WORD_1
	v_mul_f32_e32 v143, v77, v77
	v_mul_f32_e32 v199, v79, v79
	v_fmac_f32_e32 v143, v76, v76
	v_fmac_f32_e32 v199, v78, v78
	v_add_f32_e32 v143, v143, v199
	v_add_f32_e32 v141, v141, v143
	v_and_b32_sdwa v143, v78, v198 dst_sel:DWORD dst_unused:UNUSED_PAD src0_sel:WORD_1 src1_sel:DWORD
	v_add3_u32 v78, v78, v143, s71
	ds_bpermute_b32 v143, v160, v141
	v_and_b32_sdwa v199, v76, v198 dst_sel:DWORD dst_unused:UNUSED_PAD src0_sel:WORD_1 src1_sel:DWORD
	v_add3_u32 v199, v76, v199, s71
	v_and_b32_sdwa v76, v79, v198 dst_sel:DWORD dst_unused:UNUSED_PAD src0_sel:WORD_1 src1_sel:DWORD
	v_and_b32_sdwa v200, v77, v198 dst_sel:DWORD dst_unused:UNUSED_PAD src0_sel:WORD_1 src1_sel:DWORD
	v_add3_u32 v76, v79, v76, s71
	v_add3_u32 v79, v77, v200, s71
	v_and_b32_e32 v200, 0xffff0000, v76
	s_waitcnt lgkmcnt(0)
	v_add_f32_e32 v76, v141, v143
	ds_bpermute_b32 v77, v161, v76
	v_lshl_add_u64 v[210:211], v[150:151], 0, s[58:59]
	v_add_co_u32_e32 v210, vcc, s72, v210
	v_and_b32_e32 v141, 0xffff0000, v79
	s_nop 0
	v_addc_co_u32_e32 v211, vcc, 0, v211, vcc
	v_or_b32_sdwa v79, v200, v78 dst_sel:DWORD dst_unused:UNUSED_PAD src0_sel:DWORD src1_sel:WORD_1
	v_or_b32_sdwa v78, v141, v199 dst_sel:DWORD dst_unused:UNUSED_PAD src0_sel:DWORD src1_sel:WORD_1
	s_lshr_b32 s32, s58, 5
	v_add_u32_e32 v241, s32, v240
	ds_write_b64 v241, v[208:209]
	ds_write_b64 v241, v[78:79] offset:512
	s_and_saveexec_b64 s[60:61], s[10:11]
	s_cbranch_execz .LBB0_787
	v_add_u32_e32 v78, 0, v139
	s_waitcnt lgkmcnt(0)
	v_add_f32_e32 v76, v76, v77
	ds_write_b32 v78, v76
	s_branch .LBB0_787
